# baseline (speedup 1.0000x reference)
.LBB15_21:
	s_mul_i32 s6, s23, 0x222
	v_subrev_u32_e32 v153, s6, v170
	v_mfma_f32_32x32x16_f16 v[66:81], v[250:253], v[194:197], v[66:81]
	s_and_b32 s7, s19, 1
	s_mulk_i32 s7, 0x6000
	v_mfma_f32_32x32x16_f16 v[2:17], v[174:177], v[238:241], v[2:17]
	v_lshrrev_b32_e32 v173, 2, v153
	s_and_b32 s6, s23, 1
	v_mfma_f32_32x32x16_f16 v[34:49], v[174:177], v[242:245], v[34:49]
	s_mul_i32 s23, s23, 0xffff7780
	s_add_i32 s7, s7, 0x13700
	v_mfma_f32_32x32x16_f16 v[34:49], v[250:253], v[238:241], v[34:49]
	v_bitop3_b32 v174, v173, v159, 3 bitop3:0x6c
	v_add_u32_e32 v234, s18, v171
	v_bitop3_b32 v173, v173, v160, 3 bitop3:0x6c
	s_mul_i32 s6, s6, 0x9b80
	v_add_u32_e32 v154, s23, v172
	v_lshl_or_b32 v155, v169, 4, s7
	v_lshl_add_u32 v174, v174, 4, v234
	v_lshl_add_u32 v173, v173, 4, v234
	v_add3_u32 v182, v174, s6, v154
	v_add3_u32 v173, v173, s6, v154
	v_add_u32_e32 v155, v155, v168
	ds_read_b128 v[174:177], v182
	ds_read_b128 v[178:181], v173
	ds_read_b128 v[182:185], v182 offset:2048
	ds_read_b128 v[186:189], v173 offset:2048
	ds_read_b128 v[190:193], v155
	v_lshl_or_b32 v173, v165, 4, s7
	v_add_u32_e32 v173, v173, v168
	ds_read_b128 v[194:197], v173
	s_waitcnt lgkmcnt(1)
	v_mfma_f32_32x32x16_f16 v[82:97], v[190:193], v[174:177], v[82:97]
	ds_read_b128 v[198:201], v155 offset:2048
	ds_read_b128 v[202:205], v173 offset:2048
	v_add_u32_e32 v206, 1, v153
	v_lshrrev_b32_e32 v210, 2, v206
	v_bitop3_b32 v206, v210, v159, 3 bitop3:0x6c
	v_bitop3_b32 v210, v210, v160, 3 bitop3:0x6c
	v_lshl_add_u32 v206, v206, 4, v234
	v_mfma_f32_32x32x16_f16 v[114:129], v[190:193], v[178:181], v[114:129]
	v_lshl_add_u32 v210, v210, 4, v234
	v_add3_u32 v214, v206, s6, v154
	v_add3_u32 v218, v210, s6, v154
	ds_read_b128 v[206:209], v214 offset:64
	ds_read_b128 v[210:213], v218 offset:64
	v_add_u32_e32 v153, 2, v153
	v_lshrrev_b32_e32 v153, 2, v153
	s_waitcnt lgkmcnt(4)
	v_mfma_f32_32x32x16_f16 v[114:129], v[194:197], v[174:177], v[114:129]
	ds_read_b128 v[214:217], v214 offset:2112
	ds_read_b128 v[218:221], v218 offset:2112
	s_add_i32 s19, s19, 1
	v_mfma_f32_32x32x16_f16 v[50:65], v[190:193], v[182:185], v[50:65]
	ds_read_b128 v[222:225], v155 offset:8192
	ds_read_b128 v[226:229], v173 offset:8192
	v_mfma_f32_32x32x16_f16 v[98:113], v[190:193], v[186:189], v[98:113]
	ds_read_b128 v[190:193], v155 offset:10240
	ds_read_b128 v[230:233], v173 offset:10240
	v_mfma_f32_32x32x16_f16 v[98:113], v[194:197], v[182:185], v[98:113]
	v_bitop3_b32 v194, v153, v159, 3 bitop3:0x6c
	v_bitop3_b32 v153, v153, v160, 3 bitop3:0x6c
	v_lshl_add_u32 v194, v194, 4, v234
	v_lshl_add_u32 v153, v153, 4, v234
	v_add3_u32 v238, v194, s6, v154
	v_add3_u32 v153, v153, s6, v154
	ds_read_b128 v[194:197], v238 offset:128
	ds_read_b128 v[234:237], v153 offset:128
	s_waitcnt lgkmcnt(11)
	v_mfma_f32_32x32x16_f16 v[18:33], v[198:201], v[174:177], v[18:33]
	ds_read_b128 v[238:241], v238 offset:2176
	ds_read_b128 v[242:245], v153 offset:2176
	s_and_b32 s6, s19, 1
	s_mul_i32 s12, s6, 0x6000
	s_add_i32 s12, s12, 0x13700
	v_lshl_add_u32 v153, v162, 4, s12
	v_mfma_f32_32x32x16_f16 v[66:81], v[198:201], v[178:181], v[66:81]
	ds_read_b128 v[178:181], v155 offset:16384
	ds_read_b128 v[246:249], v173 offset:16384
	s_waitcnt lgkmcnt(14)
	v_mfma_f32_32x32x16_f16 v[66:81], v[202:205], v[174:177], v[66:81]
	ds_read_b128 v[174:177], v155 offset:18432
	ds_read_b128 v[250:253], v173 offset:18432
	v_mfma_f32_32x32x16_f16 v[2:17], v[198:201], v[182:185], v[2:17]
	s_waitcnt vmcnt(1)
	ds_write_b128 v153, v[142:145]
	v_lshl_add_u32 v142, v163, 4, s12
	s_waitcnt vmcnt(0)
	ds_write_b128 v142, v[146:149]
	s_mov_b64 s[26:27], exec
	s_and_b64 exec, s[26:27], s[2:3]
	v_lshl_add_u32 v142, v164, 4, s12
	ds_write_b128 v142, v[130:133]
	s_mov_b64 exec, s[26:27]
	s_and_b32 s30, s22, 1
	s_mul_i32 s30, s30, 0x9b80
	v_cmp_gt_i32_e32 vcc, s21, v152
	v_lshrrev_b32_e32 v130, 4, v152
	s_and_b64 s[28:29], vcc, s[4:5]
	s_and_b64 exec, s[26:27], s[28:29]
	v_bitop3_b32 v131, v130, v152, 3 bitop3:0x6c
	v_lshl_add_u32 v131, v131, 4, s30
	ds_write_b128 v131, v[138:141]
	s_mov_b64 exec, s[26:27]
	v_add_u32_e32 v131, s20, v0
	v_cmp_gt_i32_e32 vcc, s21, v131
	s_and_b64 s[28:29], vcc, s[4:5]
	s_and_b64 exec, s[26:27], s[28:29]
	v_bitop3_b32 v130, v130, v131, 3 bitop3:0x6c
	v_lshl_add_u32 v130, v130, 4, s30
	ds_write_b128 v130, v[134:137]
	s_mov_b64 exec, s[26:27]
	s_nop 0
	v_mfma_f32_32x32x16_f16 v[34:49], v[198:201], v[186:189], v[34:49]
	v_mfma_f32_32x32x16_f16 v[34:49], v[202:205], v[182:185], v[34:49]
	s_waitcnt lgkmcnt(15)
	v_mfma_f32_32x32x16_f16 v[82:97], v[222:225], v[206:209], v[82:97]
	v_mfma_f32_32x32x16_f16 v[114:129], v[222:225], v[210:213], v[114:129]
	s_waitcnt lgkmcnt(15)
	v_mfma_f32_32x32x16_f16 v[114:129], v[226:229], v[206:209], v[114:129]
	v_mfma_f32_32x32x16_f16 v[50:65], v[222:225], v[214:217], v[50:65]
	v_mfma_f32_32x32x16_f16 v[98:113], v[222:225], v[218:221], v[98:113]
	v_mfma_f32_32x32x16_f16 v[98:113], v[226:229], v[214:217], v[98:113]
	s_waitcnt lgkmcnt(14)
	v_mfma_f32_32x32x16_f16 v[18:33], v[190:193], v[206:209], v[18:33]
	v_mfma_f32_32x32x16_f16 v[66:81], v[190:193], v[210:213], v[66:81]
	s_waitcnt lgkmcnt(13)
	v_mfma_f32_32x32x16_f16 v[66:81], v[230:233], v[206:209], v[66:81]
	v_mfma_f32_32x32x16_f16 v[2:17], v[190:193], v[214:217], v[2:17]
	v_mfma_f32_32x32x16_f16 v[34:49], v[190:193], v[218:221], v[34:49]
	v_mfma_f32_32x32x16_f16 v[34:49], v[230:233], v[214:217], v[34:49]
	s_branch .LBB15_12
